# P5 epilogue: residual-row loads without the non-temporal hint
# speedup vs baseline: 1.0060x; 1.0060x over previous
.LBB0_636:
	v_lshl_add_u32 v6, s24, 8, v188
	v_lshl_or_b32 v2, s48, 8, v190
	v_readlane_b32 s48, v254, 13
	v_ashrrev_i32_e32 v3, 31, v2
	v_readlane_b32 s49, v254, 14
	v_ashrrev_i32_e32 v7, 31, v6
	v_lshlrev_b64 v[4:5], 13, v[6:7]
	v_lshl_add_u64 v[8:9], v[2:3], 2, s[48:49]
	s_nop 11
	v_lshl_add_u64 v[4:5], v[8:9], 0, v[4:5]
	global_load_dwordx4 v[12:15], v[4:5], off
	global_load_dwordx4 v[20:23], v[4:5], off offset:64
	global_load_dwordx4 v[24:27], v[4:5], off offset:512
	global_load_dwordx4 v[28:31], v[4:5], off offset:576
	v_or_b32_e32 v4, 16, v6
	v_ashrrev_i32_e32 v5, 31, v4
	v_lshlrev_b64 v[10:11], 13, v[4:5]
	v_lshl_add_u64 v[16:17], v[8:9], 0, v[10:11]
	global_load_dwordx4 v[180:183], v[16:17], off
	global_load_dwordx4 v[184:187], v[16:17], off offset:64
	global_load_dwordx4 v[194:197], v[16:17], off offset:512
	global_load_dwordx4 v[198:201], v[16:17], off offset:576
	v_or_b32_e32 v32, 32, v6
	v_or_b32_e32 v10, 48, v6
	v_ashrrev_i32_e32 v33, 31, v32
	v_ashrrev_i32_e32 v11, 31, v10
	v_lshlrev_b64 v[202:203], 12, v[6:7]
	v_lshlrev_b64 v[18:19], 1, v[2:3]
	v_lshlrev_b64 v[2:3], 13, v[32:33]
	v_lshlrev_b64 v[16:17], 13, v[10:11]
	v_lshl_add_u64 v[202:203], s[4:5], 0, v[202:203]
	v_lshlrev_b64 v[230:231], 12, v[4:5]
	v_lshl_add_u64 v[2:3], v[8:9], 0, v[2:3]
	v_lshl_add_u64 v[4:5], v[8:9], 0, v[16:17]
	v_lshl_add_u64 v[16:17], v[202:203], 0, v[18:19]
	global_load_dwordx4 v[202:205], v[2:3], off
	global_load_dwordx4 v[206:209], v[2:3], off offset:64
	global_load_dwordx4 v[210:213], v[2:3], off offset:512
	global_load_dwordx4 v[214:217], v[2:3], off offset:576
	global_load_dwordx4 v[218:221], v[4:5], off
	global_load_dwordx4 v[222:225], v[4:5], off offset:64
	global_load_dwordx4 v[226:229], v[4:5], off offset:512
	s_nop 0
	global_load_dwordx4 v[2:5], v[4:5], off offset:576
	v_lshl_add_u64 v[16:17], v[16:17], 0, v[170:171]
	v_lshl_add_u64 v[16:17], v[16:17], 0, v[178:179]
	s_and_b64 vcc, exec, s[6:7]
	s_mov_b64 s[6:7], -1
	v_readlane_b32 s50, v254, 15
	v_readlane_b32 s51, v254, 16
	v_readlane_b32 s52, v254, 17
	v_readlane_b32 s53, v254, 18
	v_readlane_b32 s54, v254, 19
	v_readlane_b32 s55, v254, 20
	v_readlane_b32 s56, v254, 21
	v_readlane_b32 s57, v254, 22
	v_readlane_b32 s58, v254, 23
	v_readlane_b32 s59, v254, 24
	v_readlane_b32 s60, v254, 25
	v_readlane_b32 s61, v254, 26
	v_readlane_b32 s62, v254, 27
	v_readlane_b32 s63, v254, 28
	s_waitcnt vmcnt(0)
	v_pk_mul_f32 v[14:15], v[14:15], s[12:13] op_sel_hi:[1,0]
	v_pk_mul_f32 v[12:13], v[12:13], s[12:13] op_sel_hi:[1,0]
	v_pk_mul_f32 v[22:23], v[22:23], s[12:13] op_sel_hi:[1,0]
	v_pk_mul_f32 v[20:21], v[20:21], s[12:13] op_sel_hi:[1,0]
	v_pk_fma_f32 v[14:15], v[160:161], s[14:15], v[14:15] op_sel_hi:[1,0,1]
	v_pk_fma_f32 v[12:13], v[158:159], s[14:15], v[12:13] op_sel_hi:[1,0,1]
	v_pk_fma_f32 v[22:23], v[156:157], s[14:15], v[22:23] op_sel_hi:[1,0,1]
	v_pk_fma_f32 v[20:21], v[154:155], s[14:15], v[20:21] op_sel_hi:[1,0,1]
	v_cvt_pk_bf16_f32 v12, v12, v13
	v_cvt_pk_bf16_f32 v13, v14, v15
	v_pk_mul_f32 v[26:27], v[26:27], s[12:13] op_sel_hi:[1,0]
	v_cvt_pk_bf16_f32 v14, v20, v21
	v_cvt_pk_bf16_f32 v15, v22, v23
	v_pk_mul_f32 v[24:25], v[24:25], s[12:13] op_sel_hi:[1,0]
	v_pk_mul_f32 v[30:31], v[30:31], s[12:13] op_sel_hi:[1,0]
	v_pk_mul_f32 v[28:29], v[28:29], s[12:13] op_sel_hi:[1,0]
	v_permlane16_swap_b32_e32 v12, v14
	v_permlane16_swap_b32_e32 v13, v15
	v_pk_fma_f32 v[26:27], v[152:153], s[14:15], v[26:27] op_sel_hi:[1,0,1]
	v_pk_fma_f32 v[24:25], v[150:151], s[14:15], v[24:25] op_sel_hi:[1,0,1]
	v_pk_fma_f32 v[30:31], v[144:145], s[14:15], v[30:31] op_sel_hi:[1,0,1]
	v_pk_fma_f32 v[28:29], v[142:143], s[14:15], v[28:29] op_sel_hi:[1,0,1]
	global_store_dwordx4 v[16:17], v[12:15], off
	v_pk_mul_f32 v[142:143], v[182:183], s[12:13] op_sel_hi:[1,0]
	v_pk_mul_f32 v[144:145], v[180:181], s[12:13] op_sel_hi:[1,0]
	v_cvt_pk_bf16_f32 v12, v24, v25
	v_cvt_pk_bf16_f32 v13, v26, v27
	v_cvt_pk_bf16_f32 v14, v28, v29
	v_cvt_pk_bf16_f32 v15, v30, v31
	v_pk_mul_f32 v[150:151], v[186:187], s[12:13] op_sel_hi:[1,0]
	v_permlane16_swap_b32_e32 v12, v14
	v_permlane16_swap_b32_e32 v13, v15
	global_store_dwordx4 v[16:17], v[12:15], off offset:256
	v_lshl_add_u64 v[16:17], s[4:5], 0, v[230:231]
	v_pk_mul_f32 v[152:153], v[184:185], s[12:13] op_sel_hi:[1,0]
	v_lshl_add_u64 v[16:17], v[16:17], 0, v[18:19]
	v_pk_fma_f32 v[20:21], v[148:149], s[14:15], v[142:143] op_sel_hi:[1,0,1]
	v_pk_fma_f32 v[22:23], v[146:147], s[14:15], v[144:145] op_sel_hi:[1,0,1]
	v_pk_fma_f32 v[140:141], v[140:141], s[14:15], v[150:151] op_sel_hi:[1,0,1]
	v_pk_fma_f32 v[138:139], v[138:139], s[14:15], v[152:153] op_sel_hi:[1,0,1]
	v_cvt_pk_bf16_f32 v12, v22, v23
	v_cvt_pk_bf16_f32 v13, v20, v21
	v_lshl_add_u64 v[16:17], v[16:17], 0, v[170:171]
	v_cvt_pk_bf16_f32 v14, v138, v139
	v_cvt_pk_bf16_f32 v15, v140, v141
	v_lshl_add_u64 v[16:17], v[16:17], 0, v[178:179]
	v_permlane16_swap_b32_e32 v12, v14
	v_permlane16_swap_b32_e32 v13, v15
	global_store_dwordx4 v[16:17], v[12:15], off
	v_pk_mul_f32 v[4:5], v[4:5], s[12:13] op_sel_hi:[1,0]
	v_pk_mul_f32 v[2:3], v[2:3], s[12:13] op_sel_hi:[1,0]
	v_pk_mul_f32 v[12:13], v[196:197], s[12:13] op_sel_hi:[1,0]
	v_pk_mul_f32 v[14:15], v[194:195], s[12:13] op_sel_hi:[1,0]
	v_pk_fma_f32 v[20:21], v[136:137], s[14:15], v[12:13] op_sel_hi:[1,0,1]
	v_pk_fma_f32 v[12:13], v[134:135], s[14:15], v[14:15] op_sel_hi:[1,0,1]
	v_pk_mul_f32 v[14:15], v[200:201], s[12:13] op_sel_hi:[1,0]
	v_cvt_pk_bf16_f32 v12, v12, v13
	v_cvt_pk_bf16_f32 v13, v20, v21
	v_pk_mul_f32 v[20:21], v[198:199], s[12:13] op_sel_hi:[1,0]
	v_pk_fma_f32 v[22:23], v[128:129], s[14:15], v[14:15] op_sel_hi:[1,0,1]
	v_pk_fma_f32 v[14:15], v[126:127], s[14:15], v[20:21] op_sel_hi:[1,0,1]
	v_add_u32_e32 v134, 0x80, v6
	v_cvt_pk_bf16_f32 v14, v14, v15
	v_cvt_pk_bf16_f32 v15, v22, v23
	v_pk_fma_f32 v[4:5], v[100:101], s[14:15], v[4:5] op_sel_hi:[1,0,1]
	v_permlane16_swap_b32_e32 v12, v14
	v_permlane16_swap_b32_e32 v13, v15
	global_store_dwordx4 v[16:17], v[12:15], off offset:256
	v_lshlrev_b64 v[16:17], 12, v[32:33]
	v_lshl_add_u64 v[16:17], s[4:5], 0, v[16:17]
	v_pk_mul_f32 v[12:13], v[204:205], s[12:13] op_sel_hi:[1,0]
	v_pk_mul_f32 v[14:15], v[202:203], s[12:13] op_sel_hi:[1,0]
	v_pk_fma_f32 v[20:21], v[132:133], s[14:15], v[12:13] op_sel_hi:[1,0,1]
	v_pk_fma_f32 v[12:13], v[130:131], s[14:15], v[14:15] op_sel_hi:[1,0,1]
	v_pk_mul_f32 v[14:15], v[208:209], s[12:13] op_sel_hi:[1,0]
	v_cvt_pk_bf16_f32 v12, v12, v13
	v_cvt_pk_bf16_f32 v13, v20, v21
	v_pk_mul_f32 v[20:21], v[206:207], s[12:13] op_sel_hi:[1,0]
	v_pk_fma_f32 v[22:23], v[124:125], s[14:15], v[14:15] op_sel_hi:[1,0,1]
	v_pk_fma_f32 v[14:15], v[122:123], s[14:15], v[20:21] op_sel_hi:[1,0,1]
	v_lshl_add_u64 v[16:17], v[16:17], 0, v[18:19]
	v_cvt_pk_bf16_f32 v14, v14, v15
	v_cvt_pk_bf16_f32 v15, v22, v23
	v_lshl_add_u64 v[16:17], v[16:17], 0, v[170:171]
	v_permlane16_swap_b32_e32 v12, v14
	v_permlane16_swap_b32_e32 v13, v15
	v_lshl_add_u64 v[16:17], v[16:17], 0, v[178:179]
	global_store_dwordx4 v[16:17], v[12:15], off
	v_pk_fma_f32 v[2:3], v[98:99], s[14:15], v[2:3] op_sel_hi:[1,0,1]
	v_ashrrev_i32_e32 v135, 31, v134
	v_pk_mul_f32 v[12:13], v[212:213], s[12:13] op_sel_hi:[1,0]
	v_pk_mul_f32 v[14:15], v[210:211], s[12:13] op_sel_hi:[1,0]
	v_pk_fma_f32 v[20:21], v[120:121], s[14:15], v[12:13] op_sel_hi:[1,0,1]
	v_pk_fma_f32 v[12:13], v[118:119], s[14:15], v[14:15] op_sel_hi:[1,0,1]
	v_pk_mul_f32 v[14:15], v[216:217], s[12:13] op_sel_hi:[1,0]
	v_cvt_pk_bf16_f32 v12, v12, v13
	v_cvt_pk_bf16_f32 v13, v20, v21
	v_pk_mul_f32 v[20:21], v[214:215], s[12:13] op_sel_hi:[1,0]
	v_pk_fma_f32 v[22:23], v[112:113], s[14:15], v[14:15] op_sel_hi:[1,0,1]
	v_pk_fma_f32 v[14:15], v[110:111], s[14:15], v[20:21] op_sel_hi:[1,0,1]
	v_add_u32_e32 v136, 0x90, v6
	v_cvt_pk_bf16_f32 v14, v14, v15
	v_cvt_pk_bf16_f32 v15, v22, v23
	v_ashrrev_i32_e32 v137, 31, v136
	v_permlane16_swap_b32_e32 v12, v14
	v_permlane16_swap_b32_e32 v13, v15
	global_store_dwordx4 v[16:17], v[12:15], off offset:256
	v_add_u32_e32 v138, 0xa0, v6
	v_ashrrev_i32_e32 v139, 31, v138
	v_lshlrev_b64 v[14:15], 12, v[10:11]
	v_pk_mul_f32 v[10:11], v[220:221], s[12:13] op_sel_hi:[1,0]
	v_pk_mul_f32 v[12:13], v[218:219], s[12:13] op_sel_hi:[1,0]
	v_pk_fma_f32 v[16:17], v[116:117], s[14:15], v[10:11] op_sel_hi:[1,0,1]
	v_pk_fma_f32 v[10:11], v[114:115], s[14:15], v[12:13] op_sel_hi:[1,0,1]
	v_pk_mul_f32 v[12:13], v[224:225], s[12:13] op_sel_hi:[1,0]
	v_cvt_pk_bf16_f32 v10, v10, v11
	v_cvt_pk_bf16_f32 v11, v16, v17
	v_pk_mul_f32 v[16:17], v[222:223], s[12:13] op_sel_hi:[1,0]
	v_lshl_add_u64 v[14:15], s[4:5], 0, v[14:15]
	v_pk_fma_f32 v[20:21], v[108:109], s[14:15], v[12:13] op_sel_hi:[1,0,1]
	v_pk_fma_f32 v[12:13], v[106:107], s[14:15], v[16:17] op_sel_hi:[1,0,1]
	v_lshl_add_u64 v[14:15], v[14:15], 0, v[18:19]
	v_cvt_pk_bf16_f32 v12, v12, v13
	v_cvt_pk_bf16_f32 v13, v20, v21
	v_lshl_add_u64 v[14:15], v[14:15], 0, v[170:171]
	v_permlane16_swap_b32_e32 v10, v12
	v_permlane16_swap_b32_e32 v11, v13
	v_lshl_add_u64 v[14:15], v[14:15], 0, v[178:179]
	global_store_dwordx4 v[14:15], v[10:13], off
	v_add_u32_e32 v20, 0xb0, v6
	v_ashrrev_i32_e32 v21, 31, v20
	v_pk_mul_f32 v[10:11], v[228:229], s[12:13] op_sel_hi:[1,0]
	v_pk_mul_f32 v[12:13], v[226:227], s[12:13] op_sel_hi:[1,0]
	v_pk_fma_f32 v[16:17], v[104:105], s[14:15], v[10:11] op_sel_hi:[1,0,1]
	v_pk_fma_f32 v[10:11], v[102:103], s[14:15], v[12:13] op_sel_hi:[1,0,1]
	s_nop 0
	v_cvt_pk_bf16_f32 v10, v10, v11
	v_cvt_pk_bf16_f32 v11, v16, v17
	v_cvt_pk_bf16_f32 v12, v2, v3
	v_cvt_pk_bf16_f32 v13, v4, v5
	v_lshlrev_b64 v[2:3], 13, v[134:135]
	v_permlane16_swap_b32_e32 v10, v12
	v_permlane16_swap_b32_e32 v11, v13
	global_store_dwordx4 v[14:15], v[10:13], off offset:256
	v_lshl_add_u64 v[2:3], v[8:9], 0, v[2:3]
	global_load_dwordx4 v[22:25], v[2:3], off
	global_load_dwordx4 v[26:29], v[2:3], off offset:64
	global_load_dwordx4 v[30:33], v[2:3], off offset:512
	global_load_dwordx4 v[98:101], v[2:3], off offset:576
	v_lshlrev_b64 v[2:3], 13, v[136:137]
	v_lshl_add_u64 v[2:3], v[8:9], 0, v[2:3]
	global_load_dwordx4 v[102:105], v[2:3], off
	global_load_dwordx4 v[106:109], v[2:3], off offset:64
	global_load_dwordx4 v[110:113], v[2:3], off offset:512
	global_load_dwordx4 v[114:117], v[2:3], off offset:576
	v_lshlrev_b64 v[2:3], 13, v[138:139]
	v_lshl_add_u64 v[2:3], v[8:9], 0, v[2:3]
	global_load_dwordx4 v[118:121], v[2:3], off
	global_load_dwordx4 v[122:125], v[2:3], off offset:64
	global_load_dwordx4 v[126:129], v[2:3], off offset:512
	global_load_dwordx4 v[130:133], v[2:3], off offset:576
	v_lshlrev_b64 v[2:3], 13, v[20:21]
	v_lshl_add_u64 v[2:3], v[8:9], 0, v[2:3]
	global_load_dwordx4 v[14:17], v[2:3], off
	global_load_dwordx4 v[10:13], v[2:3], off offset:64
	global_load_dwordx4 v[6:9], v[2:3], off offset:512
	s_nop 0
	global_load_dwordx4 v[2:5], v[2:3], off offset:576
	v_lshlrev_b64 v[134:135], 12, v[134:135]
	v_lshlrev_b64 v[20:21], 12, v[20:21]
	s_waitcnt vmcnt(15)
	v_pk_mul_f32 v[24:25], v[24:25], s[12:13] op_sel_hi:[1,0]
	v_pk_mul_f32 v[22:23], v[22:23], s[12:13] op_sel_hi:[1,0]
	v_pk_fma_f32 v[24:25], v[88:89], s[14:15], v[24:25] op_sel_hi:[1,0,1]
	v_pk_fma_f32 v[22:23], v[86:87], s[14:15], v[22:23] op_sel_hi:[1,0,1]
	s_waitcnt vmcnt(14)
	v_pk_mul_f32 v[26:27], v[26:27], s[12:13] op_sel_hi:[1,0]
	v_cvt_pk_bf16_f32 v22, v22, v23
	v_cvt_pk_bf16_f32 v23, v24, v25
	v_pk_mul_f32 v[24:25], v[28:29], s[12:13] op_sel_hi:[1,0]
	s_waitcnt vmcnt(3)
	v_pk_mul_f32 v[16:17], v[16:17], s[12:13] op_sel_hi:[1,0]
	v_pk_fma_f32 v[28:29], v[84:85], s[14:15], v[24:25] op_sel_hi:[1,0,1]
	v_pk_fma_f32 v[24:25], v[82:83], s[14:15], v[26:27] op_sel_hi:[1,0,1]
	v_lshl_add_u64 v[26:27], s[4:5], 0, v[134:135]
	v_lshl_add_u64 v[26:27], v[26:27], 0, v[18:19]
	v_cvt_pk_bf16_f32 v24, v24, v25
	v_cvt_pk_bf16_f32 v25, v28, v29
	v_lshl_add_u64 v[26:27], v[26:27], 0, v[170:171]
	v_permlane16_swap_b32_e32 v22, v24
	v_permlane16_swap_b32_e32 v23, v25
	v_lshl_add_u64 v[26:27], v[26:27], 0, v[178:179]
	global_store_dwordx4 v[26:27], v[22:25], off
	v_pk_mul_f32 v[14:15], v[14:15], s[12:13] op_sel_hi:[1,0]
	s_waitcnt vmcnt(3)
	v_pk_mul_f32 v[10:11], v[10:11], s[12:13] op_sel_hi:[1,0]
	v_pk_mul_f32 v[22:23], v[32:33], s[12:13] op_sel_hi:[1,0]
	v_pk_mul_f32 v[24:25], v[30:31], s[12:13] op_sel_hi:[1,0]
	v_pk_fma_f32 v[28:29], v[96:97], s[14:15], v[22:23] op_sel_hi:[1,0,1]
	v_pk_fma_f32 v[22:23], v[94:95], s[14:15], v[24:25] op_sel_hi:[1,0,1]
	v_pk_mul_f32 v[24:25], v[100:101], s[12:13] op_sel_hi:[1,0]
	v_cvt_pk_bf16_f32 v22, v22, v23
	v_cvt_pk_bf16_f32 v23, v28, v29
	v_pk_mul_f32 v[28:29], v[98:99], s[12:13] op_sel_hi:[1,0]
	v_pk_fma_f32 v[30:31], v[92:93], s[14:15], v[24:25] op_sel_hi:[1,0,1]
	v_pk_fma_f32 v[24:25], v[90:91], s[14:15], v[28:29] op_sel_hi:[1,0,1]
	v_pk_fma_f32 v[16:17], v[40:41], s[14:15], v[16:17] op_sel_hi:[1,0,1]
	v_cvt_pk_bf16_f32 v24, v24, v25
	v_cvt_pk_bf16_f32 v25, v30, v31
	v_pk_fma_f32 v[14:15], v[38:39], s[14:15], v[14:15] op_sel_hi:[1,0,1]
	v_permlane16_swap_b32_e32 v22, v24
	v_permlane16_swap_b32_e32 v23, v25
	global_store_dwordx4 v[26:27], v[22:25], off offset:256
	v_lshlrev_b64 v[26:27], 12, v[136:137]
	v_lshl_add_u64 v[26:27], s[4:5], 0, v[26:27]
	v_pk_mul_f32 v[22:23], v[104:105], s[12:13] op_sel_hi:[1,0]
	v_pk_mul_f32 v[24:25], v[102:103], s[12:13] op_sel_hi:[1,0]
	v_pk_fma_f32 v[28:29], v[72:73], s[14:15], v[22:23] op_sel_hi:[1,0,1]
	v_pk_fma_f32 v[22:23], v[70:71], s[14:15], v[24:25] op_sel_hi:[1,0,1]
	v_pk_mul_f32 v[24:25], v[108:109], s[12:13] op_sel_hi:[1,0]
	v_cvt_pk_bf16_f32 v22, v22, v23
	v_cvt_pk_bf16_f32 v23, v28, v29
	v_pk_mul_f32 v[28:29], v[106:107], s[12:13] op_sel_hi:[1,0]
	v_pk_fma_f32 v[30:31], v[68:69], s[14:15], v[24:25] op_sel_hi:[1,0,1]
	v_pk_fma_f32 v[24:25], v[66:67], s[14:15], v[28:29] op_sel_hi:[1,0,1]
	v_lshl_add_u64 v[26:27], v[26:27], 0, v[18:19]
	v_cvt_pk_bf16_f32 v24, v24, v25
	v_cvt_pk_bf16_f32 v25, v30, v31
	v_lshl_add_u64 v[26:27], v[26:27], 0, v[170:171]
	v_permlane16_swap_b32_e32 v22, v24
	v_permlane16_swap_b32_e32 v23, v25
	v_lshl_add_u64 v[26:27], v[26:27], 0, v[178:179]
	global_store_dwordx4 v[26:27], v[22:25], off
	v_pk_fma_f32 v[10:11], v[34:35], s[14:15], v[10:11] op_sel_hi:[1,0,1]
	v_pk_mul_f32 v[12:13], v[12:13], s[12:13] op_sel_hi:[1,0]
	v_pk_mul_f32 v[22:23], v[112:113], s[12:13] op_sel_hi:[1,0]
	v_pk_mul_f32 v[24:25], v[110:111], s[12:13] op_sel_hi:[1,0]
	v_pk_fma_f32 v[28:29], v[80:81], s[14:15], v[22:23] op_sel_hi:[1,0,1]
	v_pk_fma_f32 v[22:23], v[78:79], s[14:15], v[24:25] op_sel_hi:[1,0,1]
	v_pk_mul_f32 v[24:25], v[116:117], s[12:13] op_sel_hi:[1,0]
	v_cvt_pk_bf16_f32 v22, v22, v23
	v_cvt_pk_bf16_f32 v23, v28, v29
	v_pk_mul_f32 v[28:29], v[114:115], s[12:13] op_sel_hi:[1,0]
	v_pk_fma_f32 v[30:31], v[76:77], s[14:15], v[24:25] op_sel_hi:[1,0,1]
	v_pk_fma_f32 v[24:25], v[74:75], s[14:15], v[28:29] op_sel_hi:[1,0,1]
	v_pk_fma_f32 v[12:13], v[36:37], s[14:15], v[12:13] op_sel_hi:[1,0,1]
	v_cvt_pk_bf16_f32 v24, v24, v25
	v_cvt_pk_bf16_f32 v25, v30, v31
	s_waitcnt vmcnt(4)
	v_pk_mul_f32 v[8:9], v[8:9], s[12:13] op_sel_hi:[1,0]
	v_permlane16_swap_b32_e32 v22, v24
	v_permlane16_swap_b32_e32 v23, v25
	global_store_dwordx4 v[26:27], v[22:25], off offset:256
	v_lshlrev_b64 v[26:27], 12, v[138:139]
	v_lshl_add_u64 v[26:27], s[4:5], 0, v[26:27]
	v_pk_mul_f32 v[22:23], v[120:121], s[12:13] op_sel_hi:[1,0]
	v_pk_mul_f32 v[24:25], v[118:119], s[12:13] op_sel_hi:[1,0]
	v_pk_fma_f32 v[28:29], v[56:57], s[14:15], v[22:23] op_sel_hi:[1,0,1]
	v_pk_fma_f32 v[22:23], v[54:55], s[14:15], v[24:25] op_sel_hi:[1,0,1]
	v_pk_mul_f32 v[24:25], v[124:125], s[12:13] op_sel_hi:[1,0]
	v_cvt_pk_bf16_f32 v22, v22, v23
	v_cvt_pk_bf16_f32 v23, v28, v29
	v_pk_mul_f32 v[28:29], v[122:123], s[12:13] op_sel_hi:[1,0]
	v_pk_fma_f32 v[30:31], v[52:53], s[14:15], v[24:25] op_sel_hi:[1,0,1]
	v_pk_fma_f32 v[24:25], v[50:51], s[14:15], v[28:29] op_sel_hi:[1,0,1]
	v_lshl_add_u64 v[26:27], v[26:27], 0, v[18:19]
	v_cvt_pk_bf16_f32 v24, v24, v25
	v_cvt_pk_bf16_f32 v25, v30, v31
	v_lshl_add_u64 v[26:27], v[26:27], 0, v[170:171]
	v_permlane16_swap_b32_e32 v22, v24
	v_permlane16_swap_b32_e32 v23, v25
	v_lshl_add_u64 v[26:27], v[26:27], 0, v[178:179]
	global_store_dwordx4 v[26:27], v[22:25], off
	v_pk_mul_f32 v[6:7], v[6:7], s[12:13] op_sel_hi:[1,0]
	v_pk_fma_f32 v[8:9], v[48:49], s[14:15], v[8:9] op_sel_hi:[1,0,1]
	v_pk_mul_f32 v[22:23], v[128:129], s[12:13] op_sel_hi:[1,0]
	v_pk_mul_f32 v[24:25], v[126:127], s[12:13] op_sel_hi:[1,0]
	v_pk_fma_f32 v[28:29], v[64:65], s[14:15], v[22:23] op_sel_hi:[1,0,1]
	v_pk_fma_f32 v[22:23], v[62:63], s[14:15], v[24:25] op_sel_hi:[1,0,1]
	v_pk_mul_f32 v[24:25], v[132:133], s[12:13] op_sel_hi:[1,0]
	v_cvt_pk_bf16_f32 v22, v22, v23
	v_cvt_pk_bf16_f32 v23, v28, v29
	v_pk_mul_f32 v[28:29], v[130:131], s[12:13] op_sel_hi:[1,0]
	v_pk_fma_f32 v[30:31], v[60:61], s[14:15], v[24:25] op_sel_hi:[1,0,1]
	v_pk_fma_f32 v[24:25], v[58:59], s[14:15], v[28:29] op_sel_hi:[1,0,1]
	v_pk_fma_f32 v[6:7], v[46:47], s[14:15], v[6:7] op_sel_hi:[1,0,1]
	v_cvt_pk_bf16_f32 v24, v24, v25
	v_cvt_pk_bf16_f32 v25, v30, v31
	s_waitcnt vmcnt(5)
	v_pk_mul_f32 v[4:5], v[4:5], s[12:13] op_sel_hi:[1,0]
	v_permlane16_swap_b32_e32 v22, v24
	v_permlane16_swap_b32_e32 v23, v25
	global_store_dwordx4 v[26:27], v[22:25], off offset:256
	v_cvt_pk_bf16_f32 v14, v14, v15
	v_cvt_pk_bf16_f32 v15, v16, v17
	v_cvt_pk_bf16_f32 v16, v10, v11
	v_lshl_add_u64 v[10:11], s[4:5], 0, v[20:21]
	v_lshl_add_u64 v[10:11], v[10:11], 0, v[18:19]
	v_cvt_pk_bf16_f32 v17, v12, v13
	v_lshl_add_u64 v[10:11], v[10:11], 0, v[170:171]
	v_permlane16_swap_b32_e32 v14, v16
	v_permlane16_swap_b32_e32 v15, v17
	v_lshl_add_u64 v[10:11], v[10:11], 0, v[178:179]
	v_pk_mul_f32 v[2:3], v[2:3], s[12:13] op_sel_hi:[1,0]
	global_store_dwordx4 v[10:11], v[14:17], off
	v_cvt_pk_bf16_f32 v6, v6, v7
	v_cvt_pk_bf16_f32 v7, v8, v9
	v_pk_fma_f32 v[4:5], v[44:45], s[14:15], v[4:5] op_sel_hi:[1,0,1]
	v_pk_fma_f32 v[2:3], v[42:43], s[14:15], v[2:3] op_sel_hi:[1,0,1]
	s_nop 0
	v_cvt_pk_bf16_f32 v8, v2, v3
	v_cvt_pk_bf16_f32 v9, v4, v5
	s_nop 0
	v_permlane16_swap_b32_e32 v6, v8
	v_permlane16_swap_b32_e32 v7, v9
	global_store_dwordx4 v[10:11], v[6:9], off offset:256
	s_cbranch_vccnz .LBB0_625
	s_andn2_b64 vcc, exec, s[0:1]
	s_cbranch_vccnz .LBB0_624
	s_barrier
	s_branch .LBB0_624
